# speedup vs baseline: 1.0923x; 1.0923x over previous
_Z16sum_layer_kernelPKfS0_Pf:
	s_load_dwordx4 s[4:7], s[0:1], 0x0
	s_load_dwordx2 s[8:9], s[0:1], 0x10
	v_bfe_u32 v41, v0, 5, 1
	v_and_b32_e32 v40, 31, v0
	s_lshl_b32 s0, s2, 10
	v_lshlrev_b32_e32 v1, 9, v41
	v_or3_b32 v1, v1, s0, v40
	s_waitcnt lgkmcnt(0)
	s_and_b32 s13, s7, 0xffff
	s_mov_b32 s15, 0x20000
	s_mov_b32 s14, 0x200000
	s_mov_b32 s12, s6
	v_lshlrev_b32_e32 v1, 2, v1
	buffer_load_dword v18, v1, s[12:15], 0 offen nt
	buffer_load_dword v19, v1, s[12:15], 0 offen offset:128 nt
	buffer_load_dword v20, v1, s[12:15], 0 offen offset:256 nt
	buffer_load_dword v21, v1, s[12:15], 0 offen offset:384 nt
	buffer_load_dword v22, v1, s[12:15], 0 offen offset:512 nt
	buffer_load_dword v23, v1, s[12:15], 0 offen offset:640 nt
	buffer_load_dword v24, v1, s[12:15], 0 offen offset:768 nt
	buffer_load_dword v25, v1, s[12:15], 0 offen offset:896 nt
	buffer_load_dword v26, v1, s[12:15], 0 offen offset:1024 nt
	buffer_load_dword v27, v1, s[12:15], 0 offen offset:1152 nt
	buffer_load_dword v28, v1, s[12:15], 0 offen offset:1280 nt
	buffer_load_dword v29, v1, s[12:15], 0 offen offset:1408 nt
	buffer_load_dword v30, v1, s[12:15], 0 offen offset:1536 nt
	buffer_load_dword v31, v1, s[12:15], 0 offen offset:1664 nt
	buffer_load_dword v32, v1, s[12:15], 0 offen offset:1792 nt
	s_nop 0
	buffer_load_dword v1, v1, s[12:15], 0 offen offset:1920 nt
	v_lshrrev_b32_e32 v42, 6, v0
	s_lshl_b32 s0, s2, 5
	v_lshlrev_b32_e32 v3, 2, v0
	v_lshl_add_u32 v2, v42, 19, s0
	v_and_b32_e32 v34, 28, v3
	v_or_b32_e32 v2, v2, v34
	v_bfe_u32 v33, v0, 3, 3
	v_lshlrev_b32_e32 v2, 2, v2
	s_and_b32 s5, s5, 0xffff
	s_mov_b32 s6, 0x800000
	s_mov_b32 s7, s15
	v_lshl_add_u32 v35, v33, 16, v2
	s_mov_b32 s0, 0x80000
	buffer_load_dwordx4 v[2:5], v35, s[4:7], 0 offen nt
	buffer_load_dwordx4 v[6:9], v35, s[4:7], s0 offen nt
	s_mov_b32 s0, 0x100000
	s_mov_b32 s1, 0x180000
	buffer_load_dwordx4 v[10:13], v35, s[4:7], s0 offen nt
	buffer_load_dwordx4 v[14:17], v35, s[4:7], s1 offen nt
	v_and_b32_e32 v35, 63, v0
	s_waitcnt vmcnt(18)
	v_max_f32_e32 v0, v19, v19
	v_max_f32_e32 v36, v18, v18
	v_max_f32_e32 v0, v36, v0
	s_waitcnt vmcnt(16)
	v_max3_f32 v0, v0, v20, v21
	s_waitcnt vmcnt(14)
	v_max3_f32 v0, v0, v22, v23
	s_waitcnt vmcnt(12)
	v_max3_f32 v0, v0, v24, v25
	s_waitcnt vmcnt(10)
	v_max3_f32 v0, v0, v26, v27
	s_waitcnt vmcnt(8)
	v_max3_f32 v0, v0, v28, v29
	s_waitcnt vmcnt(6)
	v_max3_f32 v0, v0, v30, v31
	s_waitcnt vmcnt(4)
	v_max3_f32 v0, v0, v32, v1
	v_mov_b32_e32 v36, v0
	s_nop 1
	v_permlane32_swap_b32_e32 v0, v36
	v_max_f32_e32 v36, v36, v36
	v_max_f32_e32 v0, v0, v0
	v_max_f32_e32 v0, v0, v36
	v_mov_b32_e32 v36, 0xc1600000
	s_mov_b32 s0, 0x3fb8aa3b
	v_fmamk_f32 v0, v0, 0x3fb8aa3b, v36
	v_fma_f32 v18, v18, s0, -v0
	v_exp_f32_e32 v37, v18
	v_fma_f32 v18, v19, s0, -v0
	v_exp_f32_e32 v38, v18
	v_fma_f32 v18, v20, s0, -v0
	v_exp_f32_e32 v20, v18
	v_fma_f32 v18, v21, s0, -v0
	v_exp_f32_e32 v21, v18
	v_fma_f32 v19, v22, s0, -v0
	v_add_f32_e32 v18, 0, v37
	v_exp_f32_e32 v22, v19
	v_fma_f32 v19, v23, s0, -v0
	v_add_f32_e32 v18, v18, v38
	v_exp_f32_e32 v39, v19
	v_fma_f32 v19, v24, s0, -v0
	v_add_f32_e32 v18, v18, v20
	v_exp_f32_e32 v23, v19
	v_fma_f32 v19, v25, s0, -v0
	v_add_f32_e32 v18, v18, v21
	v_exp_f32_e32 v24, v19
	v_fma_f32 v19, v26, s0, -v0
	v_add_f32_e32 v18, v18, v22
	v_exp_f32_e32 v43, v19
	v_fma_f32 v19, v27, s0, -v0
	v_add_f32_e32 v18, v18, v39
	v_exp_f32_e32 v44, v19
	v_fma_f32 v19, v28, s0, -v0
	v_add_f32_e32 v18, v18, v23
	v_exp_f32_e32 v45, v19
	v_fma_f32 v19, v29, s0, -v0
	v_add_f32_e32 v18, v18, v24
	v_exp_f32_e32 v46, v19
	v_fma_f32 v19, v30, s0, -v0
	v_add_f32_e32 v18, v18, v43
	v_exp_f32_e32 v47, v19
	v_fma_f32 v19, v31, s0, -v0
	v_add_f32_e32 v18, v18, v44
	v_exp_f32_e32 v48, v19
	v_fma_f32 v19, v32, s0, -v0
	v_add_f32_e32 v18, v18, v45
	v_exp_f32_e32 v49, v19
	v_fma_f32 v0, v1, s0, -v0
	v_add_f32_e32 v18, v18, v46
	v_exp_f32_e32 v50, v0
	v_add_f32_e32 v0, v18, v47
	v_add_f32_e32 v0, v0, v48
	v_add_f32_e32 v0, v0, v49
	v_add_f32_e32 v0, v0, v50
	v_mov_b32_e32 v1, v0
	s_nop 1
	v_permlane32_swap_b32_e32 v0, v1
	v_add_f32_e32 v0, v0, v1
	v_log_f32_e32 v0, v0
	s_nop 0
	v_add_f32_e32 v0, 0x41600000, v0
	v_mul_f32_e32 v25, 0xbf317218, v0
	v_mul_u32_u24_e32 v0, 0x1200, v42
	v_mul_u32_u24_e32 v1, 0x90, v33
	v_lshlrev_b32_e32 v18, 2, v34
	v_add3_u32 v1, v0, v1, v18
	s_waitcnt vmcnt(3)
	ds_write_b128 v1, v[2:5]
	s_waitcnt vmcnt(2)
	ds_write_b128 v1, v[6:9] offset:1152
	s_waitcnt vmcnt(1)
	ds_write_b128 v1, v[10:13] offset:2304
	s_waitcnt vmcnt(0)
	ds_write_b128 v1, v[14:17] offset:3456
	v_mul_u32_u24_e32 v1, 0x90, v40
	v_lshlrev_b32_e32 v2, 6, v41
	v_add3_u32 v12, v0, v1, v2
	ds_read_b128 v[0:3], v12
	ds_read_b128 v[4:7], v12 offset:16
	ds_read_b128 v[8:11], v12 offset:32
	ds_read_b128 v[16:19], v12 offset:48
	v_cmp_gt_u32_e32 vcc, 32, v35
	s_waitcnt lgkmcnt(3)
	v_max_f32_e32 v12, v1, v1
	v_max_f32_e32 v13, v0, v0
	v_max_f32_e32 v12, v13, v12
	v_max3_f32 v12, v12, v2, v3
	s_waitcnt lgkmcnt(2)
	v_max3_f32 v12, v12, v4, v5
	v_max3_f32 v12, v12, v6, v7
	s_waitcnt lgkmcnt(1)
	v_max3_f32 v12, v12, v8, v9
	v_max3_f32 v12, v12, v10, v11
	s_waitcnt lgkmcnt(0)
	v_max3_f32 v12, v12, v16, v17
	v_max3_f32 v12, v12, v18, v19
	v_mov_b32_e32 v13, v12
	s_nop 1
	v_permlane32_swap_b32_e32 v12, v13
	v_max_f32_e32 v13, v13, v13
	v_max_f32_e32 v12, v12, v12
	v_max_f32_e32 v12, v12, v13
	v_fmac_f32_e32 v36, 0x3fb8aa3b, v12
	v_fma_f32 v0, v0, s0, -v36
	v_cndmask_b32_e64 v13, v25, 1.0, vcc
	v_exp_f32_e32 v25, v0
	v_fma_f32 v0, v1, s0, -v36
	v_exp_f32_e32 v26, v0
	v_fma_f32 v0, v2, s0, -v36
	v_exp_f32_e32 v27, v0
	v_fma_f32 v0, v3, s0, -v36
	v_exp_f32_e32 v28, v0
	v_fma_f32 v0, v4, s0, -v36
	v_exp_f32_e32 v29, v0
	v_fma_f32 v0, v5, s0, -v36
	v_exp_f32_e32 v30, v0
	v_fma_f32 v0, v6, s0, -v36
	v_exp_f32_e32 v31, v0
	v_fma_f32 v0, v7, s0, -v36
	v_exp_f32_e32 v32, v0
	v_fma_f32 v16, v16, s0, -v36
	v_fma_f32 v0, v8, s0, -v36
	v_exp_f32_e32 v34, v16
	v_fma_f32 v16, v17, s0, -v36
	v_exp_f32_e32 v51, v0
	v_fma_f32 v0, v9, s0, -v36
	v_exp_f32_e32 v54, v16
	v_fma_f32 v16, v18, s0, -v36
	v_exp_f32_e32 v52, v0
	v_fma_f32 v0, v10, s0, -v36
	v_exp_f32_e32 v35, v16
	v_fma_f32 v16, v19, s0, -v36
	v_exp_f32_e32 v33, v0
	v_fma_f32 v0, v11, s0, -v36
	v_exp_f32_e32 v36, v16
	v_cvt_pk_f16_f32 v19, v31, v32
	v_cvt_pk_f16_f32 v18, v29, v30
	v_cvt_pk_f16_f32 v17, v27, v28
	v_cvt_pk_f16_f32 v16, v25, v26
	v_cndmask_b32_e32 v1, 1.0, v12, vcc
	v_exp_f32_e32 v53, v0
	v_cvt_pk_f16_f32 v23, v23, v24
	v_cvt_pk_f16_f32 v22, v22, v39
	v_cvt_pk_f16_f32 v21, v20, v21
	v_cvt_pk_f16_f32 v20, v37, v38
	v_cvt_pk_f16_f32 v35, v35, v36
	v_cvt_pk_f16_f32 v34, v34, v54
	v_mfma_f32_32x32x16_f16 v[16:31], v[16:19], v[20:23], 0
	v_cvt_pk_f16_f32 v33, v33, v53
	v_cvt_pk_f16_f32 v32, v51, v52
	v_cvt_pk_f16_f32 v39, v49, v50
	v_cvt_pk_f16_f32 v38, v47, v48
	v_cvt_pk_f16_f32 v37, v45, v46
	v_cvt_pk_f16_f32 v36, v43, v44
	s_lshl_b32 s0, s2, 7
	v_mfma_f32_32x32x2_f32 v[0:15], v1, v13, 0
	v_mfma_f32_32x32x16_f16 v[16:31], v[32:35], v[36:39], v[16:31]
	v_lshl_add_u32 v32, v42, 21, s0
	v_lshl_add_u32 v32, v41, 18, v32
	v_lshl_or_b32 v32, v40, 2, v32
	s_nop 8
	v_log_f32_e32 v16, v16
	v_log_f32_e32 v17, v17
	s_nop 2
	v_fmamk_f32 v0, v16, 0x3f317218, v0
	global_store_dword v32, v0, s[8:9]
	v_fmamk_f32 v0, v17, 0x3f317218, v1
	v_log_f32_e32 v1, v18
	v_add_u32_e32 v16, 0x10000, v32
	global_store_dword v16, v0, s[8:9]
	v_log_f32_e32 v0, v19
	v_fmamk_f32 v1, v1, 0x3f317218, v2
	v_add_u32_e32 v2, 0x20000, v32
	global_store_dword v2, v1, s[8:9]
	v_fmamk_f32 v0, v0, 0x3f317218, v3
	v_log_f32_e32 v1, v20
	v_add_u32_e32 v2, 0x30000, v32
	global_store_dword v2, v0, s[8:9]
	v_log_f32_e32 v0, v21
	v_fmamk_f32 v1, v1, 0x3f317218, v4
	v_add_u32_e32 v2, 0x80000, v32
	global_store_dword v2, v1, s[8:9]
	v_fmamk_f32 v0, v0, 0x3f317218, v5
	v_log_f32_e32 v1, v22
	v_add_u32_e32 v2, 0x90000, v32
	global_store_dword v2, v0, s[8:9]
	v_log_f32_e32 v0, v23
	v_fmamk_f32 v1, v1, 0x3f317218, v6
	v_add_u32_e32 v2, 0xa0000, v32
	global_store_dword v2, v1, s[8:9]
	v_fmamk_f32 v0, v0, 0x3f317218, v7
	v_log_f32_e32 v1, v24
	v_add_u32_e32 v2, 0xb0000, v32
	global_store_dword v2, v0, s[8:9]
	v_log_f32_e32 v0, v25
	v_fmamk_f32 v1, v1, 0x3f317218, v8
	v_add_u32_e32 v2, 0x100000, v32
	global_store_dword v2, v1, s[8:9]
	v_fmamk_f32 v0, v0, 0x3f317218, v9
	v_log_f32_e32 v1, v26
	v_add_u32_e32 v2, 0x110000, v32
	global_store_dword v2, v0, s[8:9]
	v_log_f32_e32 v0, v27
	v_fmamk_f32 v1, v1, 0x3f317218, v10
	v_add_u32_e32 v2, 0x120000, v32
	global_store_dword v2, v1, s[8:9]
	v_fmamk_f32 v0, v0, 0x3f317218, v11
	v_log_f32_e32 v1, v28
	v_add_u32_e32 v2, 0x130000, v32
	global_store_dword v2, v0, s[8:9]
	v_log_f32_e32 v0, v29
	v_fmamk_f32 v1, v1, 0x3f317218, v12
	v_add_u32_e32 v2, 0x180000, v32
	global_store_dword v2, v1, s[8:9]
	v_fmamk_f32 v0, v0, 0x3f317218, v13
	v_add_u32_e32 v2, 0x190000, v32
	v_log_f32_e32 v1, v30
	global_store_dword v2, v0, s[8:9]
	v_log_f32_e32 v0, v31
	v_add_u32_e32 v2, 0x1a0000, v32
	v_fmamk_f32 v1, v1, 0x3f317218, v14
	global_store_dword v2, v1, s[8:9]
	v_fmac_f32_e32 v15, 0x3f317218, v0
	v_add_u32_e32 v0, 0x1b0000, v32
	global_store_dword v0, v15, s[8:9]
	s_endpgm
